# hand-written absmax phase: all sampled chunks of both layers in flight per wave, one atomic per workgroup and tensor
# speedup vs baseline: 1.0167x; 1.0167x over previous
.LBB0_5:
	s_or_b64 exec, exec, s[4:5]
	s_cmp_lt_i32 s42, 1
	s_cselect_b64 s[4:5], -1, 0
	s_cmp_gt_i32 s43, 0
	s_cselect_b64 s[6:7], -1, 0
	s_and_b64 s[4:5], s[4:5], s[6:7]
	s_andn2_b64 vcc, exec, s[4:5]
	s_mov_b32 s21, 0
	s_cbranch_vccnz .LBB0_302
	v_mov_b32 v8, v0
	v_mov_b32 v1, v0
	s_load_dword s33, s[0:1], 0xf8
	s_load_dwordx2 s[16:17], s[0:1], 0x48
	v_and_b32_e32 v23, 63, v1
	v_mbcnt_lo_u32_b32 v1, -1, 0
	v_mbcnt_hi_u32_b32 v3, -1, v1
	v_and_b32_e32 v1, 64, v3
	v_add_u32_e32 v4, 64, v1
	v_xor_b32_e32 v1, 1, v3
	v_cmp_lt_i32_e32 vcc, v1, v4
	v_xor_b32_e32 v5, 2, v3
	s_lshl_b32 s64, s2, 9
	v_cndmask_b32_e32 v1, v3, v1, vcc
	v_cmp_lt_i32_e32 vcc, v5, v4
	s_add_u32 s12, s0, 0xf8
	s_addc_u32 s13, s1, 0
	v_cndmask_b32_e32 v5, v3, v5, vcc
	v_lshlrev_b32_e32 v18, 2, v5
	v_xor_b32_e32 v5, 4, v3
	v_cmp_lt_i32_e32 vcc, v5, v4
	s_waitcnt lgkmcnt(0)
	s_lshl_b32 s14, s33, 9
	s_add_u32 s18, s40, 0xc000
	v_cndmask_b32_e32 v5, v3, v5, vcc
	v_lshlrev_b32_e32 v19, 2, v5
	v_xor_b32_e32 v5, 8, v3
	v_cmp_lt_i32_e32 vcc, v5, v4
	s_addc_u32 s19, s41, 0
	s_add_u32 s52, s40, 0xc008
	v_cndmask_b32_e32 v5, v3, v5, vcc
	v_lshlrev_b32_e32 v20, 2, v5
	v_xor_b32_e32 v5, 16, v3
	v_cmp_lt_i32_e32 vcc, v5, v4
	s_addc_u32 s53, s41, 0
	s_add_u32 s54, s40, 0xc110
	v_cndmask_b32_e32 v5, v3, v5, vcc
	v_lshlrev_b32_e32 v21, 2, v5
	v_xor_b32_e32 v5, 32, v3
	v_cmp_lt_i32_e32 vcc, v5, v4
	s_addc_u32 s55, s41, 0
	v_add_u32_e32 v2, s64, v8
	v_cndmask_b32_e32 v3, v3, v5, vcc
	s_add_u32 s56, s40, 0xc198
	s_mov_b32 s4, 0x1e4000
	v_lshlrev_b32_e32 v22, 2, v3
	v_ashrrev_i32_e32 v3, 31, v2
	s_mov_b32 s8, 0x80000
	s_mov_b32 s10, 0x20000
	s_addc_u32 s57, s41, 0
	v_mov_b32_e32 v5, 0
	v_mov_b32_e32 v4, v2
	s_ashr_i32 s15, s14, 31
	v_and_b32_e32 v12, 63, v8
	v_cmp_gt_u32_e64 s[6:7], s4, v2
	v_lshlrev_b32_e32 v1, 2, v1
	v_cmp_eq_u32_e64 s[4:5], 0, v23
	v_cmp_gt_u32_e64 s[8:9], s8, v2
	v_cmp_gt_u32_e64 s[10:11], s10, v2
	v_mov_b64_e32 v[6:7], v[4:5]
	v_lshl_add_u64 v[8:9], v[4:5], 4, s[16:17]
	s_lshl_b64 s[22:23], s[14:15], 4
	v_lshlrev_b64 v[10:11], 3, v[2:3]
	s_lshl_b64 s[24:25], s[14:15], 3
	s_mov_b64 s[34:35], 0
	s_mov_b64 s[46:47], -1
	s_mov_b64 s[26:27], 0x1e3fff
	s_mov_b64 s[28:29], 0x7ffff
	s_mov_b64 s[30:31], 0x1ffff
	v_lshlrev_b32_e32 v4, 4, v12
	s_mov_b64 exec, -1
	v_lshrrev_b32_e32 v1, 6, v0
	v_and_b32_e32 v2, 63, v0
	v_lshlrev_b32_e32 v3, 2, v0
	v_readfirstlane_b32 s4, v1
	s_load_dwordx2 s[70:71], s[0:1], 0x48
	s_load_dwordx2 s[72:73], s[0:1], 0xa8
	s_load_dwordx2 s[74:75], s[0:1], 0xb0
	s_load_dwordx2 s[76:77], s[0:1], 0xa0
	s_load_dwordx2 s[78:79], s[0:1], 0xc8
	s_load_dwordx2 s[80:81], s[0:1], 0xd0
	s_load_dwordx2 s[82:83], s[0:1], 0xd8
	v_lshlrev_b32_e32 v2, 4, v2
	s_lshl_b32 s5, s2, 3
	s_add_u32 s5, s5, s4
	s_lshl_b32 s6, s33, 3
	s_waitcnt lgkmcnt(0)
	s_mov_b64 s[22:23], s[70:71]
	s_mov_b32 s30, s5
	s_min_u32 s31, s30, 0x78ff
	s_lshl_b32 s31, s31, 10
	s_add_u32 s34, s22, s31
	s_addc_u32 s35, s23, 0
	global_load_dwordx4 v[4:7], v2, s[34:35]
	s_add_u32 s30, s30, s6
	s_min_u32 s31, s30, 0x78ff
	s_lshl_b32 s31, s31, 10
	s_add_u32 s34, s22, s31
	s_addc_u32 s35, s23, 0
	global_load_dwordx4 v[8:11], v2, s[34:35]
	s_add_u32 s30, s30, s6
	s_min_u32 s31, s30, 0x78ff
	s_lshl_b32 s31, s31, 10
	s_add_u32 s34, s22, s31
	s_addc_u32 s35, s23, 0
	global_load_dwordx4 v[12:15], v2, s[34:35]
	s_add_u32 s30, s30, s6
	s_min_u32 s31, s30, 0x78ff
	s_lshl_b32 s31, s31, 10
	s_add_u32 s34, s22, s31
	s_addc_u32 s35, s23, 0
	global_load_dwordx4 v[16:19], v2, s[34:35]
	s_add_u32 s30, s30, s6
	s_min_u32 s31, s30, 0x78ff
	s_lshl_b32 s31, s31, 10
	s_add_u32 s34, s22, s31
	s_addc_u32 s35, s23, 0
	global_load_dwordx4 v[20:23], v2, s[34:35]
	s_add_u32 s30, s30, s6
	s_min_u32 s31, s30, 0x78ff
	s_lshl_b32 s31, s31, 10
	s_add_u32 s34, s22, s31
	s_addc_u32 s35, s23, 0
	global_load_dwordx4 v[24:27], v2, s[34:35]
	s_add_u32 s30, s30, s6
	s_min_u32 s31, s30, 0x78ff
	s_lshl_b32 s31, s31, 10
	s_add_u32 s34, s22, s31
	s_addc_u32 s35, s23, 0
	global_load_dwordx4 v[28:31], v2, s[34:35]
	s_add_u32 s30, s30, s6
	s_min_u32 s31, s30, 0x78ff
	s_lshl_b32 s31, s31, 10
	s_add_u32 s34, s22, s31
	s_addc_u32 s35, s23, 0
	global_load_dwordx4 v[32:35], v2, s[34:35]
	s_add_u32 s30, s30, s6
	s_min_u32 s31, s30, 0x78ff
	s_lshl_b32 s31, s31, 10
	s_add_u32 s34, s22, s31
	s_addc_u32 s35, s23, 0
	global_load_dwordx4 v[36:39], v2, s[34:35]
	s_add_u32 s30, s30, s6
	s_min_u32 s31, s30, 0x78ff
	s_lshl_b32 s31, s31, 10
	s_add_u32 s34, s22, s31
	s_addc_u32 s35, s23, 0
	global_load_dwordx4 v[40:43], v2, s[34:35]
	s_add_u32 s30, s30, s6
	s_min_u32 s31, s30, 0x78ff
	s_lshl_b32 s31, s31, 10
	s_add_u32 s34, s22, s31
	s_addc_u32 s35, s23, 0
	global_load_dwordx4 v[44:47], v2, s[34:35]
	s_add_u32 s30, s30, s6
	s_min_u32 s31, s30, 0x78ff
	s_lshl_b32 s31, s31, 10
	s_add_u32 s34, s22, s31
	s_addc_u32 s35, s23, 0
	global_load_dwordx4 v[48:51], v2, s[34:35]
	s_add_u32 s30, s30, s6
	s_min_u32 s31, s30, 0x78ff
	s_lshl_b32 s31, s31, 10
	s_add_u32 s34, s22, s31
	s_addc_u32 s35, s23, 0
	global_load_dwordx4 v[52:55], v2, s[34:35]
	s_add_u32 s30, s30, s6
	s_min_u32 s31, s30, 0x78ff
	s_lshl_b32 s31, s31, 10
	s_add_u32 s34, s22, s31
	s_addc_u32 s35, s23, 0
	global_load_dwordx4 v[56:59], v2, s[34:35]
	s_add_u32 s30, s30, s6
	s_min_u32 s31, s30, 0x78ff
	s_lshl_b32 s31, s31, 10
	s_add_u32 s34, s22, s31
	s_addc_u32 s35, s23, 0
	global_load_dwordx4 v[60:63], v2, s[34:35]
	s_add_u32 s30, s30, s6
	s_min_u32 s31, s30, 0x78ff
	s_lshl_b32 s31, s31, 10
	s_add_u32 s34, s22, s31
	s_addc_u32 s35, s23, 0
	global_load_dwordx4 v[64:67], v2, s[34:35]
	s_add_u32 s30, s30, s6
	s_mov_b64 s[24:25], s[72:73]
	s_mov_b32 s30, s5
	s_min_u32 s31, s30, 0x1fff
	s_lshl_b32 s31, s31, 13
	s_add_u32 s34, s24, s31
	s_addc_u32 s35, s25, 0
	global_load_dwordx4 v[68:71], v2, s[34:35]
	s_add_u32 s30, s30, s6
	s_min_u32 s31, s30, 0x1fff
	s_lshl_b32 s31, s31, 13
	s_add_u32 s34, s24, s31
	s_addc_u32 s35, s25, 0
	global_load_dwordx4 v[72:75], v2, s[34:35]
	s_add_u32 s30, s30, s6
	s_min_u32 s31, s30, 0x1fff
	s_lshl_b32 s31, s31, 13
	s_add_u32 s34, s24, s31
	s_addc_u32 s35, s25, 0
	global_load_dwordx4 v[76:79], v2, s[34:35]
	s_add_u32 s30, s30, s6
	s_min_u32 s31, s30, 0x1fff
	s_lshl_b32 s31, s31, 13
	s_add_u32 s34, s24, s31
	s_addc_u32 s35, s25, 0
	global_load_dwordx4 v[80:83], v2, s[34:35]
	s_add_u32 s30, s30, s6
	s_mov_b64 s[26:27], s[74:75]
	s_mov_b32 s30, s5
	s_min_u32 s31, s30, 0x7ff
	s_lshl_b32 s31, s31, 13
	s_add_u32 s34, s26, s31
	s_addc_u32 s35, s27, 0
	global_load_dwordx4 v[84:87], v2, s[34:35]
	s_add_u32 s30, s30, s6
	s_mov_b64 s[28:29], s[76:77]
	s_mov_b32 s30, s5
	s_min_u32 s31, s30, 0x7ff
	s_lshl_b32 s31, s31, 13
	s_add_u32 s34, s28, s31
	s_addc_u32 s35, s29, 0
	global_load_dwordx4 v[88:91], v2, s[34:35]
	s_add_u32 s30, s30, s6
	s_add_u32 s46, s70, 0x1e40000
	s_addc_u32 s47, s71, 0
	s_mov_b32 s30, s5
	s_min_u32 s31, s30, 0x78ff
	s_lshl_b32 s31, s31, 10
	s_add_u32 s34, s46, s31
	s_addc_u32 s35, s47, 0
	global_load_dwordx4 v[92:95], v2, s[34:35]
	s_add_u32 s30, s30, s6
	s_min_u32 s31, s30, 0x78ff
	s_lshl_b32 s31, s31, 10
	s_add_u32 s34, s46, s31
	s_addc_u32 s35, s47, 0
	global_load_dwordx4 v[96:99], v2, s[34:35]
	s_add_u32 s30, s30, s6
	s_min_u32 s31, s30, 0x78ff
	s_lshl_b32 s31, s31, 10
	s_add_u32 s34, s46, s31
	s_addc_u32 s35, s47, 0
	global_load_dwordx4 v[100:103], v2, s[34:35]
	s_add_u32 s30, s30, s6
	s_min_u32 s31, s30, 0x78ff
	s_lshl_b32 s31, s31, 10
	s_add_u32 s34, s46, s31
	s_addc_u32 s35, s47, 0
	global_load_dwordx4 v[104:107], v2, s[34:35]
	s_add_u32 s30, s30, s6
	s_min_u32 s31, s30, 0x78ff
	s_lshl_b32 s31, s31, 10
	s_add_u32 s34, s46, s31
	s_addc_u32 s35, s47, 0
	global_load_dwordx4 v[108:111], v2, s[34:35]
	s_add_u32 s30, s30, s6
	s_min_u32 s31, s30, 0x78ff
	s_lshl_b32 s31, s31, 10
	s_add_u32 s34, s46, s31
	s_addc_u32 s35, s47, 0
	global_load_dwordx4 v[112:115], v2, s[34:35]
	s_add_u32 s30, s30, s6
	s_min_u32 s31, s30, 0x78ff
	s_lshl_b32 s31, s31, 10
	s_add_u32 s34, s46, s31
	s_addc_u32 s35, s47, 0
	global_load_dwordx4 v[116:119], v2, s[34:35]
	s_add_u32 s30, s30, s6
	s_min_u32 s31, s30, 0x78ff
	s_lshl_b32 s31, s31, 10
	s_add_u32 s34, s46, s31
	s_addc_u32 s35, s47, 0
	global_load_dwordx4 v[120:123], v2, s[34:35]
	s_add_u32 s30, s30, s6
	s_min_u32 s31, s30, 0x78ff
	s_lshl_b32 s31, s31, 10
	s_add_u32 s34, s46, s31
	s_addc_u32 s35, s47, 0
	global_load_dwordx4 v[124:127], v2, s[34:35]
	s_add_u32 s30, s30, s6
	s_min_u32 s31, s30, 0x78ff
	s_lshl_b32 s31, s31, 10
	s_add_u32 s34, s46, s31
	s_addc_u32 s35, s47, 0
	global_load_dwordx4 v[128:131], v2, s[34:35]
	s_add_u32 s30, s30, s6
	s_min_u32 s31, s30, 0x78ff
	s_lshl_b32 s31, s31, 10
	s_add_u32 s34, s46, s31
	s_addc_u32 s35, s47, 0
	global_load_dwordx4 v[132:135], v2, s[34:35]
	s_add_u32 s30, s30, s6
	s_min_u32 s31, s30, 0x78ff
	s_lshl_b32 s31, s31, 10
	s_add_u32 s34, s46, s31
	s_addc_u32 s35, s47, 0
	global_load_dwordx4 v[136:139], v2, s[34:35]
	s_add_u32 s30, s30, s6
	s_min_u32 s31, s30, 0x78ff
	s_lshl_b32 s31, s31, 10
	s_add_u32 s34, s46, s31
	s_addc_u32 s35, s47, 0
	global_load_dwordx4 v[140:143], v2, s[34:35]
	s_add_u32 s30, s30, s6
	s_min_u32 s31, s30, 0x78ff
	s_lshl_b32 s31, s31, 10
	s_add_u32 s34, s46, s31
	s_addc_u32 s35, s47, 0
	global_load_dwordx4 v[144:147], v2, s[34:35]
	s_add_u32 s30, s30, s6
	s_min_u32 s31, s30, 0x78ff
	s_lshl_b32 s31, s31, 10
	s_add_u32 s34, s46, s31
	s_addc_u32 s35, s47, 0
	global_load_dwordx4 v[148:151], v2, s[34:35]
	s_add_u32 s30, s30, s6
	s_min_u32 s31, s30, 0x78ff
	s_lshl_b32 s31, s31, 10
	s_add_u32 s34, s46, s31
	s_addc_u32 s35, s47, 0
	global_load_dwordx4 v[152:155], v2, s[34:35]
	s_add_u32 s30, s30, s6
	s_add_u32 s48, s72, 0x4000000
	s_addc_u32 s49, s73, 0
	s_mov_b32 s30, s5
	s_min_u32 s31, s30, 0x1fff
	s_lshl_b32 s31, s31, 13
	s_add_u32 s34, s48, s31
	s_addc_u32 s35, s49, 0
	global_load_dwordx4 v[156:159], v2, s[34:35]
	s_add_u32 s30, s30, s6
	s_min_u32 s31, s30, 0x1fff
	s_lshl_b32 s31, s31, 13
	s_add_u32 s34, s48, s31
	s_addc_u32 s35, s49, 0
	global_load_dwordx4 v[160:163], v2, s[34:35]
	s_add_u32 s30, s30, s6
	s_min_u32 s31, s30, 0x1fff
	s_lshl_b32 s31, s31, 13
	s_add_u32 s34, s48, s31
	s_addc_u32 s35, s49, 0
	global_load_dwordx4 v[164:167], v2, s[34:35]
	s_add_u32 s30, s30, s6
	s_min_u32 s31, s30, 0x1fff
	s_lshl_b32 s31, s31, 13
	s_add_u32 s34, s48, s31
	s_addc_u32 s35, s49, 0
	global_load_dwordx4 v[168:171], v2, s[34:35]
	s_add_u32 s30, s30, s6
	s_add_u32 s50, s74, 0x1000000
	s_addc_u32 s51, s75, 0
	s_mov_b32 s30, s5
	s_min_u32 s31, s30, 0x7ff
	s_lshl_b32 s31, s31, 13
	s_add_u32 s34, s50, s31
	s_addc_u32 s35, s51, 0
	global_load_dwordx4 v[172:175], v2, s[34:35]
	s_add_u32 s30, s30, s6
	s_add_u32 s52, s76, 0x1000000
	s_addc_u32 s53, s77, 0
	s_mov_b32 s30, s5
	s_min_u32 s31, s30, 0x7ff
	s_lshl_b32 s31, s31, 13
	s_add_u32 s34, s52, s31
	s_addc_u32 s35, s53, 0
	global_load_dwordx4 v[176:179], v2, s[34:35]
	s_add_u32 s30, s30, s6
	s_waitcnt vmcnt(28)
	v_mov_b32_e32 v184, 0
	v_max3_f32 v184, |v4|, |v5|, v184
	v_max3_f32 v184, |v6|, |v7|, v184
	v_max3_f32 v184, |v8|, |v9|, v184
	v_max3_f32 v184, |v10|, |v11|, v184
	v_max3_f32 v184, |v12|, |v13|, v184
	v_max3_f32 v184, |v14|, |v15|, v184
	v_max3_f32 v184, |v16|, |v17|, v184
	v_max3_f32 v184, |v18|, |v19|, v184
	v_max3_f32 v184, |v20|, |v21|, v184
	v_max3_f32 v184, |v22|, |v23|, v184
	v_max3_f32 v184, |v24|, |v25|, v184
	v_max3_f32 v184, |v26|, |v27|, v184
	v_max3_f32 v184, |v28|, |v29|, v184
	v_max3_f32 v184, |v30|, |v31|, v184
	v_max3_f32 v184, |v32|, |v33|, v184
	v_max3_f32 v184, |v34|, |v35|, v184
	v_max3_f32 v184, |v36|, |v37|, v184
	v_max3_f32 v184, |v38|, |v39|, v184
	v_max3_f32 v184, |v40|, |v41|, v184
	v_max3_f32 v184, |v42|, |v43|, v184
	v_max3_f32 v184, |v44|, |v45|, v184
	v_max3_f32 v184, |v46|, |v47|, v184
	v_max3_f32 v184, |v48|, |v49|, v184
	v_max3_f32 v184, |v50|, |v51|, v184
	v_max3_f32 v184, |v52|, |v53|, v184
	v_max3_f32 v184, |v54|, |v55|, v184
	v_max3_f32 v184, |v56|, |v57|, v184
	v_max3_f32 v184, |v58|, |v59|, v184
	v_max3_f32 v184, |v60|, |v61|, v184
	v_max3_f32 v184, |v62|, |v63|, v184
	v_max3_f32 v184, |v64|, |v65|, v184
	v_max3_f32 v184, |v66|, |v67|, v184
	s_mul_i32 s30, s6, 16
	s_add_u32 s30, s30, s5
.Labs_rem_0_0:
	s_cmp_ge_u32 s30, 0x7900
	s_cbranch_scc1 .Labs_rem_0_0_done
	s_lshl_b32 s31, s30, 10
	s_add_u32 s34, s22, s31
	s_addc_u32 s35, s23, 0
	global_load_dwordx4 v[188:191], v2, s[34:35]
	s_add_u32 s30, s30, s6
	s_waitcnt vmcnt(0)
	v_max3_f32 v184, |v188|, |v189|, v184
	v_max3_f32 v184, |v190|, |v191|, v184
	s_branch .Labs_rem_0_0
.Labs_rem_0_0_done:
	ds_write_b32 v3, v184 offset:0
	s_waitcnt vmcnt(24)
	v_mov_b32_e32 v184, 0
	v_max3_f32 v184, |v68|, |v69|, v184
	v_max3_f32 v184, |v70|, |v71|, v184
	v_max3_f32 v184, |v72|, |v73|, v184
	v_max3_f32 v184, |v74|, |v75|, v184
	v_max3_f32 v184, |v76|, |v77|, v184
	v_max3_f32 v184, |v78|, |v79|, v184
	v_max3_f32 v184, |v80|, |v81|, v184
	v_max3_f32 v184, |v82|, |v83|, v184
	s_mul_i32 s30, s6, 4
	s_add_u32 s30, s30, s5
.Labs_rem_0_1:
	s_cmp_ge_u32 s30, 0x2000
	s_cbranch_scc1 .Labs_rem_0_1_done
	s_lshl_b32 s31, s30, 13
	s_add_u32 s34, s24, s31
	s_addc_u32 s35, s25, 0
	global_load_dwordx4 v[188:191], v2, s[34:35]
	s_add_u32 s30, s30, s6
	s_waitcnt vmcnt(0)
	v_max3_f32 v184, |v188|, |v189|, v184
	v_max3_f32 v184, |v190|, |v191|, v184
	s_branch .Labs_rem_0_1
.Labs_rem_0_1_done:
	ds_write_b32 v3, v184 offset:2048
	s_waitcnt vmcnt(23)
	v_mov_b32_e32 v184, 0
	v_max3_f32 v184, |v84|, |v85|, v184
	v_max3_f32 v184, |v86|, |v87|, v184
	s_mul_i32 s30, s6, 1
	s_add_u32 s30, s30, s5
.Labs_rem_0_2:
	s_cmp_ge_u32 s30, 0x800
	s_cbranch_scc1 .Labs_rem_0_2_done
	s_lshl_b32 s31, s30, 13
	s_add_u32 s34, s26, s31
	s_addc_u32 s35, s27, 0
	global_load_dwordx4 v[188:191], v2, s[34:35]
	s_add_u32 s30, s30, s6
	s_waitcnt vmcnt(0)
	v_max3_f32 v184, |v188|, |v189|, v184
	v_max3_f32 v184, |v190|, |v191|, v184
	s_branch .Labs_rem_0_2
.Labs_rem_0_2_done:
	ds_write_b32 v3, v184 offset:4096
	s_waitcnt vmcnt(22)
	v_mov_b32_e32 v184, 0
	v_max3_f32 v184, |v88|, |v89|, v184
	v_max3_f32 v184, |v90|, |v91|, v184
	s_mul_i32 s30, s6, 1
	s_add_u32 s30, s30, s5
.Labs_rem_0_3:
	s_cmp_ge_u32 s30, 0x800
	s_cbranch_scc1 .Labs_rem_0_3_done
	s_lshl_b32 s31, s30, 13
	s_add_u32 s34, s28, s31
	s_addc_u32 s35, s29, 0
	global_load_dwordx4 v[188:191], v2, s[34:35]
	s_add_u32 s30, s30, s6
	s_waitcnt vmcnt(0)
	v_max3_f32 v184, |v188|, |v189|, v184
	v_max3_f32 v184, |v190|, |v191|, v184
	s_branch .Labs_rem_0_3
.Labs_rem_0_3_done:
	ds_write_b32 v3, v184 offset:6144
	s_waitcnt vmcnt(6)
	v_mov_b32_e32 v184, 0
	v_max3_f32 v184, |v92|, |v93|, v184
	v_max3_f32 v184, |v94|, |v95|, v184
	v_max3_f32 v184, |v96|, |v97|, v184
	v_max3_f32 v184, |v98|, |v99|, v184
	v_max3_f32 v184, |v100|, |v101|, v184
	v_max3_f32 v184, |v102|, |v103|, v184
	v_max3_f32 v184, |v104|, |v105|, v184
	v_max3_f32 v184, |v106|, |v107|, v184
	v_max3_f32 v184, |v108|, |v109|, v184
	v_max3_f32 v184, |v110|, |v111|, v184
	v_max3_f32 v184, |v112|, |v113|, v184
	v_max3_f32 v184, |v114|, |v115|, v184
	v_max3_f32 v184, |v116|, |v117|, v184
	v_max3_f32 v184, |v118|, |v119|, v184
	v_max3_f32 v184, |v120|, |v121|, v184
	v_max3_f32 v184, |v122|, |v123|, v184
	v_max3_f32 v184, |v124|, |v125|, v184
	v_max3_f32 v184, |v126|, |v127|, v184
	v_max3_f32 v184, |v128|, |v129|, v184
	v_max3_f32 v184, |v130|, |v131|, v184
	v_max3_f32 v184, |v132|, |v133|, v184
	v_max3_f32 v184, |v134|, |v135|, v184
	v_max3_f32 v184, |v136|, |v137|, v184
	v_max3_f32 v184, |v138|, |v139|, v184
	v_max3_f32 v184, |v140|, |v141|, v184
	v_max3_f32 v184, |v142|, |v143|, v184
	v_max3_f32 v184, |v144|, |v145|, v184
	v_max3_f32 v184, |v146|, |v147|, v184
	v_max3_f32 v184, |v148|, |v149|, v184
	v_max3_f32 v184, |v150|, |v151|, v184
	v_max3_f32 v184, |v152|, |v153|, v184
	v_max3_f32 v184, |v154|, |v155|, v184
	s_mul_i32 s30, s6, 16
	s_add_u32 s30, s30, s5
.Labs_rem_1_0:
	s_cmp_ge_u32 s30, 0x7900
	s_cbranch_scc1 .Labs_rem_1_0_done
	s_lshl_b32 s31, s30, 10
	s_add_u32 s34, s46, s31
	s_addc_u32 s35, s47, 0
	global_load_dwordx4 v[188:191], v2, s[34:35]
	s_add_u32 s30, s30, s6
	s_waitcnt vmcnt(0)
	v_max3_f32 v184, |v188|, |v189|, v184
	v_max3_f32 v184, |v190|, |v191|, v184
	s_branch .Labs_rem_1_0
.Labs_rem_1_0_done:
	ds_write_b32 v3, v184 offset:8192
	s_waitcnt vmcnt(2)
	v_mov_b32_e32 v184, 0
	v_max3_f32 v184, |v156|, |v157|, v184
	v_max3_f32 v184, |v158|, |v159|, v184
	v_max3_f32 v184, |v160|, |v161|, v184
	v_max3_f32 v184, |v162|, |v163|, v184
	v_max3_f32 v184, |v164|, |v165|, v184
	v_max3_f32 v184, |v166|, |v167|, v184
	v_max3_f32 v184, |v168|, |v169|, v184
	v_max3_f32 v184, |v170|, |v171|, v184
	s_mul_i32 s30, s6, 4
	s_add_u32 s30, s30, s5
.Labs_rem_1_1:
	s_cmp_ge_u32 s30, 0x2000
	s_cbranch_scc1 .Labs_rem_1_1_done
	s_lshl_b32 s31, s30, 13
	s_add_u32 s34, s48, s31
	s_addc_u32 s35, s49, 0
	global_load_dwordx4 v[188:191], v2, s[34:35]
	s_add_u32 s30, s30, s6
	s_waitcnt vmcnt(0)
	v_max3_f32 v184, |v188|, |v189|, v184
	v_max3_f32 v184, |v190|, |v191|, v184
	s_branch .Labs_rem_1_1
.Labs_rem_1_1_done:
	ds_write_b32 v3, v184 offset:10240
	s_waitcnt vmcnt(1)
	v_mov_b32_e32 v184, 0
	v_max3_f32 v184, |v172|, |v173|, v184
	v_max3_f32 v184, |v174|, |v175|, v184
	s_mul_i32 s30, s6, 1
	s_add_u32 s30, s30, s5
.Labs_rem_1_2:
	s_cmp_ge_u32 s30, 0x800
	s_cbranch_scc1 .Labs_rem_1_2_done
	s_lshl_b32 s31, s30, 13
	s_add_u32 s34, s50, s31
	s_addc_u32 s35, s51, 0
	global_load_dwordx4 v[188:191], v2, s[34:35]
	s_add_u32 s30, s30, s6
	s_waitcnt vmcnt(0)
	v_max3_f32 v184, |v188|, |v189|, v184
	v_max3_f32 v184, |v190|, |v191|, v184
	s_branch .Labs_rem_1_2
.Labs_rem_1_2_done:
	ds_write_b32 v3, v184 offset:12288
	s_waitcnt vmcnt(0)
	v_mov_b32_e32 v184, 0
	v_max3_f32 v184, |v176|, |v177|, v184
	v_max3_f32 v184, |v178|, |v179|, v184
	s_mul_i32 s30, s6, 1
	s_add_u32 s30, s30, s5
.Labs_rem_1_3:
	s_cmp_ge_u32 s30, 0x800
	s_cbranch_scc1 .Labs_rem_1_3_done
	s_lshl_b32 s31, s30, 13
	s_add_u32 s34, s52, s31
	s_addc_u32 s35, s53, 0
	global_load_dwordx4 v[188:191], v2, s[34:35]
	s_add_u32 s30, s30, s6
	s_waitcnt vmcnt(0)
	v_max3_f32 v184, |v188|, |v189|, v184
	v_max3_f32 v184, |v190|, |v191|, v184
	s_branch .Labs_rem_1_3
.Labs_rem_1_3_done:
	ds_write_b32 v3, v184 offset:14336
	v_and_b32_e32 v192, 63, v0
	s_lshl_b32 s20, s4, 9
	s_add_u32 s20, s20, 0x4000
	v_lshl_add_u32 v193, v192, 2, s20
	v_and_b32_e32 v194, 7, v192
	v_lshl_add_u32 v195, v194, 5, s20
	s_add_u32 s21, s20, 0x100
	v_lshl_add_u32 v196, v194, 2, s21
	v_mov_b32_e32 v197, s21
	s_mov_b32 s38, s5
.Labs_exp_loop:
	s_cmp_ge_u32 s38, 0xc00
	s_cbranch_scc1 .Labs_exp_done
	s_lshr_b32 s20, s38, 5
	s_mul_i32 s20, s20, 0xab
	s_lshr_b32 s20, s20, 9
	s_mul_i32 s21, s20, 0x60
	s_sub_u32 s21, s38, s21
	s_mov_b64 s[34:35], s[82:83]
	s_cmp_lt_u32 s21, 64
	s_cselect_b32 s34, s80, s34
	s_cselect_b32 s35, s81, s35
	s_cselect_b32 s39, 4, 6
	s_cmp_lt_u32 s21, 32
	s_cselect_b32 s34, s78, s34
	s_cselect_b32 s35, s79, s35
	s_add_u32 s39, s39, s21
	s_lshl_b32 s39, s39, 2
	s_and_b32 s22, s21, 31
	s_lshl_b32 s22, s22, 23
	s_add_u32 s34, s34, s22
	s_addc_u32 s35, s35, 0
	s_lshl_b32 s22, s20, 13
	s_add_u32 s34, s34, s22
	s_addc_u32 s35, s35, 0
	global_load_dwordx4 v[4:7], v2, s[34:35]
	s_add_u32 s34, s34, 0x40000
	s_addc_u32 s35, s35, 0
	global_load_dwordx4 v[8:11], v2, s[34:35]
	s_add_u32 s34, s34, 0x40000
	s_addc_u32 s35, s35, 0
	global_load_dwordx4 v[12:15], v2, s[34:35]
	s_add_u32 s34, s34, 0x40000
	s_addc_u32 s35, s35, 0
	global_load_dwordx4 v[16:19], v2, s[34:35]
	s_add_u32 s34, s34, 0x40000
	s_addc_u32 s35, s35, 0
	global_load_dwordx4 v[20:23], v2, s[34:35]
	s_add_u32 s34, s34, 0x40000
	s_addc_u32 s35, s35, 0
	global_load_dwordx4 v[24:27], v2, s[34:35]
	s_add_u32 s34, s34, 0x40000
	s_addc_u32 s35, s35, 0
	global_load_dwordx4 v[28:31], v2, s[34:35]
	s_add_u32 s34, s34, 0x40000
	s_addc_u32 s35, s35, 0
	global_load_dwordx4 v[32:35], v2, s[34:35]
	s_add_u32 s34, s34, 0x40000
	s_addc_u32 s35, s35, 0
	global_load_dwordx4 v[36:39], v2, s[34:35]
	s_add_u32 s34, s34, 0x40000
	s_addc_u32 s35, s35, 0
	global_load_dwordx4 v[40:43], v2, s[34:35]
	s_add_u32 s34, s34, 0x40000
	s_addc_u32 s35, s35, 0
	global_load_dwordx4 v[44:47], v2, s[34:35]
	s_add_u32 s34, s34, 0x40000
	s_addc_u32 s35, s35, 0
	global_load_dwordx4 v[48:51], v2, s[34:35]
	s_add_u32 s34, s34, 0x40000
	s_addc_u32 s35, s35, 0
	global_load_dwordx4 v[52:55], v2, s[34:35]
	s_add_u32 s34, s34, 0x40000
	s_addc_u32 s35, s35, 0
	global_load_dwordx4 v[56:59], v2, s[34:35]
	s_add_u32 s34, s34, 0x40000
	s_addc_u32 s35, s35, 0
	global_load_dwordx4 v[60:63], v2, s[34:35]
	s_add_u32 s34, s34, 0x40000
	s_addc_u32 s35, s35, 0
	global_load_dwordx4 v[64:67], v2, s[34:35]
	s_add_u32 s34, s34, 0x40000
	s_addc_u32 s35, s35, 0
	global_load_dwordx4 v[68:71], v2, s[34:35]
	s_add_u32 s34, s34, 0x40000
	s_addc_u32 s35, s35, 0
	global_load_dwordx4 v[72:75], v2, s[34:35]
	s_add_u32 s34, s34, 0x40000
	s_addc_u32 s35, s35, 0
	global_load_dwordx4 v[76:79], v2, s[34:35]
	s_add_u32 s34, s34, 0x40000
	s_addc_u32 s35, s35, 0
	global_load_dwordx4 v[80:83], v2, s[34:35]
	s_add_u32 s34, s34, 0x40000
	s_addc_u32 s35, s35, 0
	global_load_dwordx4 v[84:87], v2, s[34:35]
	s_add_u32 s34, s34, 0x40000
	s_addc_u32 s35, s35, 0
	global_load_dwordx4 v[88:91], v2, s[34:35]
	s_add_u32 s34, s34, 0x40000
	s_addc_u32 s35, s35, 0
	global_load_dwordx4 v[92:95], v2, s[34:35]
	s_add_u32 s34, s34, 0x40000
	s_addc_u32 s35, s35, 0
	global_load_dwordx4 v[96:99], v2, s[34:35]
	s_add_u32 s34, s34, 0x40000
	s_addc_u32 s35, s35, 0
	global_load_dwordx4 v[100:103], v2, s[34:35]
	s_add_u32 s34, s34, 0x40000
	s_addc_u32 s35, s35, 0
	global_load_dwordx4 v[104:107], v2, s[34:35]
	s_add_u32 s34, s34, 0x40000
	s_addc_u32 s35, s35, 0
	global_load_dwordx4 v[108:111], v2, s[34:35]
	s_add_u32 s34, s34, 0x40000
	s_addc_u32 s35, s35, 0
	global_load_dwordx4 v[112:115], v2, s[34:35]
	s_add_u32 s34, s34, 0x40000
	s_addc_u32 s35, s35, 0
	global_load_dwordx4 v[116:119], v2, s[34:35]
	s_add_u32 s34, s34, 0x40000
	s_addc_u32 s35, s35, 0
	global_load_dwordx4 v[120:123], v2, s[34:35]
	s_add_u32 s34, s34, 0x40000
	s_addc_u32 s35, s35, 0
	global_load_dwordx4 v[124:127], v2, s[34:35]
	s_add_u32 s34, s34, 0x40000
	s_addc_u32 s35, s35, 0
	global_load_dwordx4 v[128:131], v2, s[34:35]
	v_mov_b32_e32 v184, 0
	s_waitcnt vmcnt(24)
	v_max3_f32 v184, |v4|, |v5|, v184
	v_max3_f32 v184, |v6|, |v7|, v184
	v_max3_f32 v184, |v8|, |v9|, v184
	v_max3_f32 v184, |v10|, |v11|, v184
	v_max3_f32 v184, |v12|, |v13|, v184
	v_max3_f32 v184, |v14|, |v15|, v184
	v_max3_f32 v184, |v16|, |v17|, v184
	v_max3_f32 v184, |v18|, |v19|, v184
	v_max3_f32 v184, |v20|, |v21|, v184
	v_max3_f32 v184, |v22|, |v23|, v184
	v_max3_f32 v184, |v24|, |v25|, v184
	v_max3_f32 v184, |v26|, |v27|, v184
	v_max3_f32 v184, |v28|, |v29|, v184
	v_max3_f32 v184, |v30|, |v31|, v184
	v_max3_f32 v184, |v32|, |v33|, v184
	v_max3_f32 v184, |v34|, |v35|, v184
	s_waitcnt vmcnt(16)
	v_max3_f32 v184, |v36|, |v37|, v184
	v_max3_f32 v184, |v38|, |v39|, v184
	v_max3_f32 v184, |v40|, |v41|, v184
	v_max3_f32 v184, |v42|, |v43|, v184
	v_max3_f32 v184, |v44|, |v45|, v184
	v_max3_f32 v184, |v46|, |v47|, v184
	v_max3_f32 v184, |v48|, |v49|, v184
	v_max3_f32 v184, |v50|, |v51|, v184
	v_max3_f32 v184, |v52|, |v53|, v184
	v_max3_f32 v184, |v54|, |v55|, v184
	v_max3_f32 v184, |v56|, |v57|, v184
	v_max3_f32 v184, |v58|, |v59|, v184
	v_max3_f32 v184, |v60|, |v61|, v184
	v_max3_f32 v184, |v62|, |v63|, v184
	v_max3_f32 v184, |v64|, |v65|, v184
	v_max3_f32 v184, |v66|, |v67|, v184
	s_waitcnt vmcnt(8)
	v_max3_f32 v184, |v68|, |v69|, v184
	v_max3_f32 v184, |v70|, |v71|, v184
	v_max3_f32 v184, |v72|, |v73|, v184
	v_max3_f32 v184, |v74|, |v75|, v184
	v_max3_f32 v184, |v76|, |v77|, v184
	v_max3_f32 v184, |v78|, |v79|, v184
	v_max3_f32 v184, |v80|, |v81|, v184
	v_max3_f32 v184, |v82|, |v83|, v184
	v_max3_f32 v184, |v84|, |v85|, v184
	v_max3_f32 v184, |v86|, |v87|, v184
	v_max3_f32 v184, |v88|, |v89|, v184
	v_max3_f32 v184, |v90|, |v91|, v184
	v_max3_f32 v184, |v92|, |v93|, v184
	v_max3_f32 v184, |v94|, |v95|, v184
	v_max3_f32 v184, |v96|, |v97|, v184
	v_max3_f32 v184, |v98|, |v99|, v184
	s_waitcnt vmcnt(0)
	v_max3_f32 v184, |v100|, |v101|, v184
	v_max3_f32 v184, |v102|, |v103|, v184
	v_max3_f32 v184, |v104|, |v105|, v184
	v_max3_f32 v184, |v106|, |v107|, v184
	v_max3_f32 v184, |v108|, |v109|, v184
	v_max3_f32 v184, |v110|, |v111|, v184
	v_max3_f32 v184, |v112|, |v113|, v184
	v_max3_f32 v184, |v114|, |v115|, v184
	v_max3_f32 v184, |v116|, |v117|, v184
	v_max3_f32 v184, |v118|, |v119|, v184
	v_max3_f32 v184, |v120|, |v121|, v184
	v_max3_f32 v184, |v122|, |v123|, v184
	v_max3_f32 v184, |v124|, |v125|, v184
	v_max3_f32 v184, |v126|, |v127|, v184
	v_max3_f32 v184, |v128|, |v129|, v184
	v_max3_f32 v184, |v130|, |v131|, v184
	ds_write_b32 v193, v184
	ds_read_b128 v[200:203], v195
	ds_read_b128 v[204:207], v195 offset:16
	s_waitcnt lgkmcnt(0)
	v_max3_f32 v184, v200, v201, v202
	v_max3_f32 v184, v184, v203, v204
	v_max3_f32 v184, v184, v205, v206
	v_max_f32_e32 v184, v184, v207
	ds_write_b32 v196, v184
	ds_read_b128 v[200:203], v197
	ds_read_b128 v[204:207], v197 offset:16
	s_waitcnt lgkmcnt(0)
	v_max3_f32 v184, v200, v201, v202
	v_max3_f32 v184, v184, v203, v204
	v_max3_f32 v184, v184, v205, v206
	v_max_f32_e32 v184, v184, v207
	v_mov_b32_e32 v198, s39
	s_mov_b64 exec, 1
	global_atomic_umax v198, v184, s[18:19]
	s_mov_b64 exec, -1
	s_add_u32 s38, s38, s6
	s_branch .Labs_exp_loop
.Labs_exp_done:
	s_waitcnt lgkmcnt(0)
	s_barrier
	s_lshl_b32 s20, s4, 11
	v_lshl_add_u32 v199, v192, 5, s20
	ds_read_b128 v[200:203], v199
	ds_read_b128 v[204:207], v199 offset:16
	s_waitcnt lgkmcnt(0)
	v_max3_f32 v184, v200, v201, v202
	v_max3_f32 v184, v184, v203, v204
	v_max3_f32 v184, v184, v205, v206
	v_max_f32_e32 v184, v184, v207
	ds_write_b32 v193, v184
	ds_read_b128 v[200:203], v195
	ds_read_b128 v[204:207], v195 offset:16
	s_waitcnt lgkmcnt(0)
	v_max3_f32 v184, v200, v201, v202
	v_max3_f32 v184, v184, v203, v204
	v_max3_f32 v184, v184, v205, v206
	v_max_f32_e32 v184, v184, v207
	ds_write_b32 v196, v184
	ds_read_b128 v[200:203], v197
	ds_read_b128 v[204:207], v197 offset:16
	s_waitcnt lgkmcnt(0)
	v_max3_f32 v184, v200, v201, v202
	v_max3_f32 v184, v184, v203, v204
	v_max3_f32 v184, v184, v205, v206
	v_max_f32_e32 v184, v184, v207
	s_lshr_b32 s20, s4, 2
	s_and_b32 s21, s4, 3
	s_cmp_eq_u32 s21, 1
	s_cselect_b32 s22, 2, 0
	s_cmp_eq_u32 s21, 2
	s_cselect_b32 s22, 0x44, s22
	s_cmp_eq_u32 s21, 3
	s_cselect_b32 s22, 0x66, s22
	s_add_u32 s22, s22, s20
	s_lshl_b32 s22, s22, 2
	v_mov_b32_e32 v198, s22
	s_mov_b64 exec, 1
	global_atomic_umax v198, v184, s[18:19]
	s_mov_b64 exec, -1
.LBB0_51:
	s_waitcnt vmcnt(0)
	s_waitcnt lgkmcnt(0)
	s_barrier
	s_and_saveexec_b64 s[4:5], s[36:37]
	s_cbranch_execz .LBB0_103
	s_add_i32 s6, 0, 0x23ff0
	v_mov_b32_e32 v1, s6
	s_waitcnt vmcnt(0) expcnt(0) lgkmcnt(0)
	ds_read_b32 v3, v1
	s_add_i32 s6, 0, 0x23ff4
	v_mov_b32_e32 v1, s6
	ds_read_b32 v1, v1
	s_waitcnt lgkmcnt(1)
	v_cmp_ne_u32_e32 vcc, 0, v3
	s_cbranch_vccnz .LBB0_67
	s_load_dwordx2 s[10:11], s[12:13], 0x4
	s_add_u32 s6, s40, 0x8200
	s_addc_u32 s7, s41, 0
	s_add_u32 s8, s40, 0x8400
	s_addc_u32 s9, s41, 0
	s_waitcnt lgkmcnt(0)
	s_mul_i32 s65, s10, s33
	s_add_u32 s10, s40, 0x8500
	s_mul_i32 s65, s65, s11
	s_addc_u32 s11, s41, 0
	s_add_u32 s20, s40, 0x8600
	s_addc_u32 s21, s41, 0
	s_add_u32 s22, s40, 0x8700
	s_addc_u32 s23, s41, 0
	s_add_u32 s24, s40, 0x8800
	s_addc_u32 s25, s41, 0
	s_add_u32 s26, s40, 0x8900
	s_addc_u32 s27, s41, 0
	s_add_u32 s28, s40, 0x8a00
	s_addc_u32 s29, s41, 0
	s_add_u32 s30, s40, 0x8b00
	s_addc_u32 s31, s41, 0
	s_add_u32 s34, s40, 0x8c00
	s_addc_u32 s35, s41, 0
	s_add_u32 s38, s40, 0x8d00
	s_addc_u32 s39, s41, 0
	s_add_u32 s46, s40, 0x8e00
	s_addc_u32 s47, s41, 0
	s_add_u32 s48, s40, 0x8f00
	s_addc_u32 s49, s41, 0
	s_add_u32 s50, s40, 0x9000
	s_addc_u32 s51, s41, 0
	s_add_u32 s52, s40, 0x9100
	s_addc_u32 s53, s41, 0
	s_add_u32 s54, s40, 0x9200
	s_addc_u32 s55, s41, 0
	s_add_u32 s56, s40, 0x9300
	s_addc_u32 s57, s41, 0
	s_mov_b32 s66, 1
	v_mov_b32_e32 v17, 0
	s_branch .LBB0_55
